# P3 pooling loop: dov-iteration waits relaxed (ld complete via vmcnt(12) at top, ds_write waits skipped when va/vr in flight)
# baseline (speedup 1.0000x reference)
.LBB0_470:
	v_lshl_add_u32 v57, s2, 9, v21
	s_mov_b32 s3, 0x200000
	v_cmp_gt_i32_e64 s[42:43], s3, v57
	s_or_b64 s[0:1], s[44:45], s[42:43]
	s_waitcnt lgkmcnt(0)
	s_and_saveexec_b64 s[16:17], s[0:1]
	s_cbranch_execz .LBB0_509
	v_ashrrev_i32_e32 v72, 5, v21
	s_movk_i32 s61, 0x210
	v_mul_lo_u32 v22, v72, s61
	v_add_u32_e32 v23, 0, v22
	v_lshlrev_b32_e32 v22, 4, v20
	v_and_b32_e32 v24, 0x1f0, v22
	v_add_u32_e32 v22, 0x200, v21
	v_ashrrev_i32_e32 v73, 5, v22
	v_mul_lo_u32 v22, v73, s61
	v_add_u32_e32 v25, 0, v22
	v_add_u32_e32 v22, 0x400, v21
	v_ashrrev_i32_e32 v74, 5, v22
	v_mul_lo_u32 v22, v74, s61
	v_add_u32_e32 v26, 0, v22
	v_add_u32_e32 v22, 0x600, v21
	v_ashrrev_i32_e32 v75, 5, v22
	v_mul_lo_u32 v22, v75, s61
	v_add_u32_e32 v27, 0, v22
	v_add_u32_e32 v22, 0x800, v21
	v_ashrrev_i32_e32 v76, 5, v22
	v_mul_lo_u32 v22, v76, s61
	v_add_u32_e32 v28, 0, v22
	v_lshlrev_b32_e32 v22, 3, v20
	v_mov_b32_e32 v52, 0
	v_and_b32_e32 v20, 31, v20
	v_ashrrev_i32_e32 v29, 3, v21
	v_lshlrev_b32_e32 v78, 4, v20
	v_lshlrev_b32_e32 v20, 3, v20
	v_mov_b32_e32 v21, v52
	v_and_b32_e32 v77, -4, v29
	v_lshl_add_u64 v[20:21], s[56:57], 0, v[20:21]
	s_mov_b64 s[12:13], 0x3b800000
	v_lshl_add_u64 v[54:55], v[20:21], 0, s[12:13]
	v_mul_lo_u32 v20, v77, s61
	v_or_b32_e32 v82, 3, v29
	s_lshl_b32 s35, s34, 9
	v_add_u32_e32 v79, 0, v20
	v_mul_lo_u32 v21, v82, s61
	s_add_u32 s36, s56, 0x2f800000
	s_movk_i32 s10, 0x4f
	v_and_b32_e32 v22, 0xf8, v22
	v_add_u32_e32 v20, 0x210, v79
	v_add_u32_e32 v21, 0, v21
	v_add_u32_e32 v56, 0, v78
	s_addc_u32 s37, s57, 0
	s_lshl_b32 s60, s34, 11
	v_cmp_gt_i32_e64 s[0:1], s10, v72
	s_mov_b32 s39, 0
	v_cmp_gt_i32_e64 s[4:5], s10, v73
	v_cmp_gt_i32_e64 s[6:7], s10, v74
	v_cmp_gt_i32_e64 s[8:9], s10, v75
	v_cmp_gt_i32_e64 s[10:11], s10, v76
	v_or_b32_e32 v80, 1, v77
	v_or_b32_e32 v81, 2, v77
	v_add_u32_e32 v83, 0x1080, v56
	s_lshl_b32 s62, s2, 3
	s_lshl_b32 s63, s34, 3
	s_mov_b64 s[40:41], 0
	s_movk_i32 s64, 0xf000
	s_movk_i32 s65, 0x1000
	s_movk_i32 s68, 0xfff
	v_add_u32_e32 v84, v23, v24
	v_add_u32_e32 v85, v25, v24
	v_add_u32_e32 v86, v26, v24
	v_add_u32_e32 v87, v27, v24
	v_add_u32_e32 v88, v28, v24
	v_lshlrev_b32_e32 v58, 1, v22
	v_add_u32_e32 v89, v21, v78
	v_mov_b32_e32 v90, 0xfff
	v_add_u32_e32 v91, v20, v78
	s_mov_b32 s69, s2
	v_mov_b32_e32 v20, 0
	v_mov_b32_e32 v21, v52
	v_mov_b32_e32 v22, v52
	v_mov_b32_e32 v23, v52
	v_mov_b32_e32 v28, v52
	v_mov_b32_e32 v29, v52
	v_mov_b32_e32 v30, v52
	v_mov_b32_e32 v31, v52
	v_mov_b32_e32 v36, v52
	v_mov_b32_e32 v37, v52
	v_mov_b32_e32 v38, v52
	v_mov_b32_e32 v39, v52
	v_mov_b32_e32 v44, v52
	v_mov_b32_e32 v45, v52
	v_mov_b32_e32 v46, v52
	v_mov_b32_e32 v47, v52
	v_mov_b32_e32 v24, 0
	v_mov_b32_e32 v25, v52
	v_mov_b32_e32 v26, v52
	v_mov_b32_e32 v27, v52
	v_mov_b32_e32 v32, v52
	v_mov_b32_e32 v33, v52
	v_mov_b32_e32 v34, v52
	v_mov_b32_e32 v35, v52
	v_mov_b32_e32 v40, v52
	v_mov_b32_e32 v41, v52
	v_mov_b32_e32 v42, v52
	v_mov_b32_e32 v43, v52
	v_mov_b32_e32 v48, v52
	v_mov_b32_e32 v49, v52
	v_mov_b32_e32 v50, v52
	v_mov_b32_e32 v51, v52
	s_waitcnt vmcnt(0)
	s_branch .LBB0_473

.LBB0_473:
	s_mov_b32 s99, 0
	s_and_saveexec_b64 s[12:13], s[42:43]
	s_cbranch_execz .LBB0_475
	s_mov_b32 s99, 1
	s_waitcnt vmcnt(12)
	v_bfe_u32 v20, v57, 8, 11
	v_ashrrev_i32_e32 v23, 7, v57
	v_sub_u32_e32 v22, 0, v20
	v_and_or_b32 v20, v23, s64, v20
	v_ashrrev_i32_e32 v21, 31, v20
	v_lshlrev_b64 v[20:21], 13, v[20:21]
	v_lshlrev_b32_e32 v24, 4, v57
	v_bfi_b32 v22, s68, v22, v23
	v_add_u32_e32 v36, s35, v57
	v_lshl_add_u64 v[20:21], s[14:15], 0, v[20:21]
	v_and_b32_e32 v44, 0xff0, v24
	v_mov_b32_e32 v45, v52
	v_ashrrev_i32_e32 v23, 31, v22
	v_bfe_u32 v28, v36, 8, 11
	v_ashrrev_i32_e32 v31, 7, v36
	v_lshl_add_u64 v[20:21], v[20:21], 0, v[44:45]
	v_lshlrev_b64 v[22:23], 13, v[22:23]
	v_sub_u32_e32 v30, 0, v28
	v_and_or_b32 v28, v31, s64, v28
	v_add_co_u32_e32 v20, vcc, 0x1000, v20
	v_lshl_add_u64 v[22:23], s[14:15], 0, v[22:23]
	v_ashrrev_i32_e32 v29, 31, v28
	v_addc_co_u32_e32 v21, vcc, 0, v21, vcc
	v_lshl_add_u64 v[22:23], v[22:23], 0, v[44:45]
	v_lshlrev_b64 v[28:29], 13, v[28:29]
	v_bfi_b32 v30, s68, v30, v31
	v_add_u32_e32 v46, s35, v36
	v_add_co_u32_e32 v24, vcc, 0x1000, v22
	v_lshl_add_u64 v[28:29], s[14:15], 0, v[28:29]
	v_ashrrev_i32_e32 v31, 31, v30
	v_bfe_u32 v36, v46, 8, 11
	v_ashrrev_i32_e32 v39, 7, v46
	v_addc_co_u32_e32 v25, vcc, 0, v23, vcc
	v_lshl_add_u64 v[28:29], v[28:29], 0, v[44:45]
	v_lshlrev_b64 v[30:31], 13, v[30:31]
	v_sub_u32_e32 v38, 0, v36
	v_and_or_b32 v36, v39, s64, v36
	v_add_co_u32_e32 v28, vcc, s65, v28
	v_lshl_add_u64 v[30:31], s[14:15], 0, v[30:31]
	v_ashrrev_i32_e32 v37, 31, v36
	v_addc_co_u32_e32 v29, vcc, 0, v29, vcc
	v_lshl_add_u64 v[30:31], v[30:31], 0, v[44:45]
	v_lshlrev_b64 v[36:37], 13, v[36:37]
	v_bfi_b32 v38, s68, v38, v39
	v_add_u32_e32 v46, s35, v46
	v_add_co_u32_e32 v32, vcc, s65, v30
	v_lshl_add_u64 v[36:37], s[14:15], 0, v[36:37]
	v_ashrrev_i32_e32 v39, 31, v38
	v_bfe_u32 v47, v46, 8, 11
	v_ashrrev_i32_e32 v49, 7, v46
	v_addc_co_u32_e32 v33, vcc, 0, v31, vcc
	v_lshl_add_u64 v[36:37], v[36:37], 0, v[44:45]
	v_lshlrev_b64 v[38:39], 13, v[38:39]
	v_and_or_b32 v46, v49, s64, v47
	v_add_co_u32_e32 v36, vcc, s65, v36
	v_lshl_add_u64 v[38:39], s[14:15], 0, v[38:39]
	v_sub_u32_e32 v48, 0, v47
	v_ashrrev_i32_e32 v47, 31, v46
	v_addc_co_u32_e32 v37, vcc, 0, v37, vcc
	v_lshl_add_u64 v[38:39], v[38:39], 0, v[44:45]
	v_lshlrev_b64 v[46:47], 13, v[46:47]
	v_bfi_b32 v48, s68, v48, v49
	v_add_co_u32_e32 v40, vcc, s65, v38
	v_lshl_add_u64 v[46:47], s[14:15], 0, v[46:47]
	v_ashrrev_i32_e32 v49, 31, v48
	v_addc_co_u32_e32 v41, vcc, 0, v39, vcc
	v_lshl_add_u64 v[46:47], v[46:47], 0, v[44:45]
	v_lshlrev_b64 v[48:49], 13, v[48:49]
	v_add_co_u32_e32 v46, vcc, s65, v46
	v_lshl_add_u64 v[48:49], s[14:15], 0, v[48:49]
	s_nop 0
	v_addc_co_u32_e32 v47, vcc, 0, v47, vcc
	v_lshl_add_u64 v[44:45], v[48:49], 0, v[44:45]
	v_add_co_u32_e32 v48, vcc, s65, v44
	global_load_dwordx4 v[20:23], v[20:21], off
	s_nop 0
	global_load_dwordx4 v[24:27], v[24:25], off
	v_addc_co_u32_e32 v49, vcc, 0, v45, vcc
	global_load_dwordx4 v[28:31], v[28:29], off
	s_nop 0
	global_load_dwordx4 v[32:35], v[32:33], off
	s_nop 0
	global_load_dwordx4 v[36:39], v[36:37], off
	s_nop 0
	global_load_dwordx4 v[40:43], v[40:41], off
	s_nop 0
	global_load_dwordx4 v[44:47], v[46:47], off
	s_nop 0
	global_load_dwordx4 v[48:51], v[48:49], off

.LBB0_483:
	s_cmp_lg_u32 s99, 0
	s_cbranch_scc1 .Lp3w_e
	s_waitcnt vmcnt(0)
.Lp3w_e:
	ds_write_b128 v88, v[16:19]
.LBB0_484:
	s_or_b64 exec, exec, s[44:45]
	s_add_i32 s33, s69, s34
	s_cmpk_gt_i32 s33, 0x7ff
	s_waitcnt lgkmcnt(0)
	s_barrier
	s_cbranch_scc1 .LBB0_486
	s_lshl_b32 s38, s33, 3
	s_and_b32 s44, s38, 0xfc0
	s_add_i32 s44, s44, -8
	s_cmp_lg_u32 s99, 0
	s_cbranch_scc1 .Lp3w_f
	s_waitcnt vmcnt(0)
.Lp3w_f:
	v_add_u32_e32 v0, s44, v72
	v_add_u32_e32 v2, s44, v73
	v_add_u32_e32 v8, s44, v74
	v_add_u32_e32 v10, s44, v75
	v_add_u32_e32 v16, s44, v76
	s_and_b32 s45, s38, 0xfffff000
	v_med3_i32 v0, v0, 0, v90
	v_med3_i32 v2, v2, 0, v90
	v_med3_i32 v8, v8, 0, v90
	v_med3_i32 v10, v10, 0, v90
	v_med3_i32 v16, v16, 0, v90
	v_or_b32_e32 v0, s45, v0
	v_or_b32_e32 v2, s45, v2
	v_or_b32_e32 v8, s45, v8
	v_or_b32_e32 v10, s45, v10
	v_or_b32_e32 v16, s45, v16
	v_ashrrev_i32_e32 v1, 31, v0
	v_ashrrev_i32_e32 v3, 31, v2
	v_ashrrev_i32_e32 v9, 31, v8
	v_ashrrev_i32_e32 v11, 31, v10
	v_ashrrev_i32_e32 v17, 31, v16
	v_lshlrev_b64 v[0:1], 13, v[0:1]
	s_lshl_b32 s33, s33, 9
	v_lshlrev_b64 v[2:3], 13, v[2:3]
	v_lshlrev_b64 v[8:9], 13, v[8:9]
	v_lshlrev_b64 v[10:11], 13, v[10:11]
	v_lshlrev_b64 v[16:17], 13, v[16:17]
	v_lshl_add_u64 v[0:1], s[14:15], 0, v[0:1]
	s_and_b32 s38, s33, 0xe00
	v_lshl_add_u64 v[2:3], s[14:15], 0, v[2:3]
	v_lshl_add_u64 v[8:9], s[14:15], 0, v[8:9]
	v_lshl_add_u64 v[10:11], s[14:15], 0, v[10:11]
	v_lshl_add_u64 v[16:17], s[14:15], 0, v[16:17]
	v_lshl_add_u64 v[0:1], v[0:1], 0, s[38:39]
	v_mov_b32_e32 v59, v52
	v_lshl_add_u64 v[2:3], v[2:3], 0, s[38:39]
	v_lshl_add_u64 v[8:9], v[8:9], 0, s[38:39]
	v_lshl_add_u64 v[10:11], v[10:11], 0, s[38:39]
	v_lshl_add_u64 v[16:17], v[16:17], 0, s[38:39]
	v_lshl_add_u64 v[0:1], v[0:1], 0, v[58:59]
	v_lshl_add_u64 v[4:5], v[2:3], 0, v[58:59]
	v_lshl_add_u64 v[8:9], v[8:9], 0, v[58:59]
	v_lshl_add_u64 v[12:13], v[10:11], 0, v[58:59]
	v_lshl_add_u64 v[16:17], v[16:17], 0, v[58:59]
	global_load_dwordx4 v[0:3], v[0:1], off nt
	s_nop 0
	global_load_dwordx4 v[4:7], v[4:5], off nt
	s_nop 0
	global_load_dwordx4 v[8:11], v[8:9], off nt
	s_nop 0
	global_load_dwordx4 v[12:15], v[12:13], off nt
	s_nop 0
	global_load_dwordx4 v[16:19], v[16:17], off nt

.LBB0_505:
	s_cmp_lg_u32 s99, 0
	s_cbranch_scc1 .Lp3w_a
	s_waitcnt vmcnt(4)
.Lp3w_a:
	ds_write_b128 v84, v[0:3]
	s_or_b64 exec, exec, s[44:45]
	s_and_saveexec_b64 s[44:45], s[4:5]
	s_cbranch_execz .LBB0_480
.LBB0_506:
	s_cmp_lg_u32 s99, 0
	s_cbranch_scc1 .Lp3w_b
	s_waitcnt vmcnt(3)
.Lp3w_b:
	ds_write_b128 v85, v[4:7]
	s_or_b64 exec, exec, s[44:45]
	s_and_saveexec_b64 s[44:45], s[6:7]
	s_cbranch_execz .LBB0_481
.LBB0_507:
	s_cmp_lg_u32 s99, 0
	s_cbranch_scc1 .Lp3w_c
	s_waitcnt vmcnt(2)
.Lp3w_c:
	ds_write_b128 v86, v[8:11]
	s_or_b64 exec, exec, s[44:45]
	s_and_saveexec_b64 s[44:45], s[8:9]
	s_cbranch_execz .LBB0_482
.LBB0_508:
	s_cmp_lg_u32 s99, 0
	s_cbranch_scc1 .Lp3w_d
	s_waitcnt vmcnt(1)
.Lp3w_d:
	ds_write_b128 v87, v[12:15]
	s_or_b64 exec, exec, s[44:45]
	s_and_saveexec_b64 s[44:45], s[10:11]
	s_cbranch_execnz .LBB0_483
	s_branch .LBB0_484
